# MOE1: per-unit bias vectors prefetched into LDS by LDS-DMA before the K-loop (epilogue reads LDS instead of 4 global loads + vmcnt(0)); tile count via LDS; conversion steps rebalanced 44/60
# baseline (speedup 1.0000x reference)
.LBB0_223:
	s_andn2_b64 vcc, exec, s[6:7]
	s_cbranch_vccnz .LBB0_230
	s_waitcnt vmcnt(0)
	s_barrier
	s_load_dwordx2 s[6:7], s[90:91], 0xa8
	s_load_dwordx2 s[8:9], s[90:91], 0xb8
	s_load_dwordx2 s[10:11], s[90:91], 0xc8
	v_readlane_b32 s2, v254, 19
	s_mov_b32 s16, 2
	s_lshr_b32 s101, s2, 3
	s_and_b32 s2, s2, 7
	s_lshr_b32 vcc_lo, s41, 3
	s_movk_i32 vcc_hi, 0x3000
	s_cmp_lg_u32 vcc_lo, 0x100
	s_cbranch_scc1 .Lcv_gen
	s_cmp_lt_u32 s101, 0xc0
	s_cbranch_scc0 .Lcv_hi
	s_mov_b32 vcc_lo, 0xc0
	s_movk_i32 vcc_hi, 0x2100
	s_branch .Lcv_gen
.Lcv_hi:
	s_add_i32 s101, s101, 0x2040
	s_mov_b32 vcc_lo, 64
.Lcv_gen:
	v_mbcnt_lo_u32_b32 v128, -1, 0
	v_mbcnt_hi_u32_b32 v128, -1, v128
	s_lshl_b32 s12, s2, 17
	v_lshlrev_b32_e32 v129, 4, v128
	v_add_u32_e32 v129, s12, v129
	v_mov_b32_e32 v220, v129
	v_add_u32_e32 v221, 0x2000, v129
	v_add_u32_e32 v222, 0x4000, v129
	v_add_u32_e32 v223, 0x6000, v129
	v_add_u32_e32 v224, 0x8000, v129
	v_add_u32_e32 v225, 0xa000, v129
	v_add_u32_e32 v226, 0xc000, v129
	v_add_u32_e32 v227, 0xe000, v129
	v_add_u32_e32 v228, 0x10000, v129
	v_add_u32_e32 v229, 0x12000, v129
	v_add_u32_e32 v230, 0x14000, v129
	v_add_u32_e32 v231, 0x16000, v129
	v_add_u32_e32 v232, 0x18000, v129
	v_add_u32_e32 v233, 0x1a000, v129
	v_add_u32_e32 v234, 0x1c000, v129
	v_add_u32_e32 v235, 0x1e000, v129
	v_and_b32_e32 v130, 7, v128
	v_xor_b32_e32 v130, s2, v130
	v_lshlrev_b32_e32 v130, 4, v130
	v_lshl_add_u32 v242, v128, 9, v130
	v_lshrrev_b32_e32 v129, 3, v128
	v_and_b32_e32 v130, 7, v128
	v_lshrrev_b32_e32 v131, 2, v129
	v_xor_b32_e32 v131, v130, v131
	v_lshlrev_b32_e32 v131, 4, v131
	s_lshl_b32 s12, s2, 5
	v_add_u32_e32 v132, s12, v129
	v_lshl_add_u32 v243, v132, 7, v131
	v_xor_b32_e32 v244, 0x20, v243
	v_xor_b32_e32 v245, 0x40, v243
	v_xor_b32_e32 v246, 0x60, v243
	v_lshlrev_b32_e32 v130, 4, v130
	v_lshl_add_u32 v133, v132, 11, v130
	v_mov_b32_e32 v236, v133
	v_add_u32_e32 v237, 0x4000, v133
	v_add_u32_e32 v238, 0x8000, v133
	v_add_u32_e32 v239, 0xc000, v133
	v_mov_b32_e32 v240, 0x42000000
	v_mov_b32_e32 v241, 0x42000000
	s_waitcnt lgkmcnt(0)
	s_mov_b32 s98, s101
	s_add_i32 s101, s101, vcc_lo
	s_cmp_lt_u32 s98, vcc_hi
	s_cbranch_scc1 .Lcv_ld_p0
	s_mov_b32 s16, 99
	s_branch .Lcv_ldskip_p0

.Lcv_ldskip_p0:
	s_mov_b32 s99, s101
	s_add_i32 s101, s101, vcc_lo
	s_cmp_lt_u32 s99, vcc_hi
	s_cbranch_scc1 .Lcv_ld_p1
	s_mov_b32 s16, 99
	s_branch .Lcv_ldskip_p1

.Lcv_ldskip_p1:
	s_mov_b32 s100, s101
	s_add_i32 s101, s101, vcc_lo
	s_cmp_lt_u32 s100, vcc_hi
	s_cbranch_scc1 .Lcv_ld_p2
	s_mov_b32 s16, 99
	s_branch .Lcv_ldskip_p2

.Lcv_ldskip_p2:
.Lcv_loop:
	s_cmp_lt_u32 s98, vcc_hi
	s_cbranch_scc0 .Lcv_done
	s_cmp_eq_u32 s16, 0
	s_cbranch_scc1 .Lcv_w40_f0
	s_cmp_eq_u32 s16, 99
	s_cbranch_scc1 .Lcv_w0_f0
	s_sub_u32 s16, s16, 1
	s_waitcnt vmcnt(32)
	s_branch .Lcv_wd_f0

.Lcv_wd_f0:
	v_pk_mul_f32 v[0:1], v[0:1], v[240:241]
	v_pk_mul_f32 v[2:3], v[2:3], v[240:241]
	v_pk_mul_f32 v[4:5], v[4:5], v[240:241]
	v_pk_mul_f32 v[6:7], v[6:7], v[240:241]
	v_pk_mul_f32 v[8:9], v[8:9], v[240:241]
	v_pk_mul_f32 v[10:11], v[10:11], v[240:241]
	v_pk_mul_f32 v[12:13], v[12:13], v[240:241]
	v_pk_mul_f32 v[14:15], v[14:15], v[240:241]
	v_pk_mul_f32 v[16:17], v[16:17], v[240:241]
	v_pk_mul_f32 v[18:19], v[18:19], v[240:241]
	v_pk_mul_f32 v[20:21], v[20:21], v[240:241]
	v_pk_mul_f32 v[22:23], v[22:23], v[240:241]
	v_pk_mul_f32 v[24:25], v[24:25], v[240:241]
	v_pk_mul_f32 v[26:27], v[26:27], v[240:241]
	v_pk_mul_f32 v[28:29], v[28:29], v[240:241]
	v_pk_mul_f32 v[30:31], v[30:31], v[240:241]
	v_pk_mul_f32 v[32:33], v[32:33], v[240:241]
	v_pk_mul_f32 v[34:35], v[34:35], v[240:241]
	v_pk_mul_f32 v[36:37], v[36:37], v[240:241]
	v_pk_mul_f32 v[38:39], v[38:39], v[240:241]
	v_pk_mul_f32 v[40:41], v[40:41], v[240:241]
	v_pk_mul_f32 v[42:43], v[42:43], v[240:241]
	v_pk_mul_f32 v[44:45], v[44:45], v[240:241]
	v_pk_mul_f32 v[46:47], v[46:47], v[240:241]
	v_pk_mul_f32 v[48:49], v[48:49], v[240:241]
	v_pk_mul_f32 v[50:51], v[50:51], v[240:241]
	v_pk_mul_f32 v[52:53], v[52:53], v[240:241]
	v_pk_mul_f32 v[54:55], v[54:55], v[240:241]
	v_pk_mul_f32 v[56:57], v[56:57], v[240:241]
	v_pk_mul_f32 v[58:59], v[58:59], v[240:241]
	v_pk_mul_f32 v[60:61], v[60:61], v[240:241]
	v_pk_mul_f32 v[62:63], v[62:63], v[240:241]
	v_cvt_pk_fp8_f32 v128, v0, v4
	v_cvt_pk_fp8_f32 v129, v1, v5
	v_cvt_pk_fp8_f32 v130, v2, v6
	v_cvt_pk_fp8_f32 v131, v3, v7
	v_cvt_pk_fp8_f32 v128, v8, v12 op_sel:[0,0,1]
	v_cvt_pk_fp8_f32 v129, v9, v13 op_sel:[0,0,1]
	v_cvt_pk_fp8_f32 v130, v10, v14 op_sel:[0,0,1]
	v_cvt_pk_fp8_f32 v131, v11, v15 op_sel:[0,0,1]
	v_cvt_pk_fp8_f32 v1, v16, v20
	v_cvt_pk_fp8_f32 v5, v17, v21
	v_cvt_pk_fp8_f32 v9, v18, v22
	v_cvt_pk_fp8_f32 v13, v19, v23
	v_cvt_pk_fp8_f32 v2, v32, v36
	v_cvt_pk_fp8_f32 v6, v33, v37
	v_cvt_pk_fp8_f32 v10, v34, v38
	v_cvt_pk_fp8_f32 v14, v35, v39
	v_cvt_pk_fp8_f32 v3, v48, v52
	v_cvt_pk_fp8_f32 v7, v49, v53
	v_cvt_pk_fp8_f32 v11, v50, v54
	v_cvt_pk_fp8_f32 v15, v51, v55
	v_cvt_pk_fp8_f32 v1, v24, v28 op_sel:[0,0,1]
	v_cvt_pk_fp8_f32 v5, v25, v29 op_sel:[0,0,1]
	v_cvt_pk_fp8_f32 v9, v26, v30 op_sel:[0,0,1]
	v_cvt_pk_fp8_f32 v13, v27, v31 op_sel:[0,0,1]
	v_cvt_pk_fp8_f32 v2, v40, v44 op_sel:[0,0,1]
	v_cvt_pk_fp8_f32 v6, v41, v45 op_sel:[0,0,1]
	v_cvt_pk_fp8_f32 v10, v42, v46 op_sel:[0,0,1]
	v_cvt_pk_fp8_f32 v14, v43, v47 op_sel:[0,0,1]
	v_cvt_pk_fp8_f32 v3, v56, v60 op_sel:[0,0,1]
	v_cvt_pk_fp8_f32 v7, v57, v61 op_sel:[0,0,1]
	v_cvt_pk_fp8_f32 v11, v58, v62 op_sel:[0,0,1]
	v_cvt_pk_fp8_f32 v15, v59, v63 op_sel:[0,0,1]
	v_mov_b32_e32 v0, v128
	v_mov_b32_e32 v4, v129
	v_mov_b32_e32 v8, v130
	v_mov_b32_e32 v12, v131
	s_cmp_lt_u32 s98, 0x1000
	s_mov_b32 s0, 0x24000000
	s_cselect_b32 s0, 0x14000000, s0
	s_cmp_lt_u32 s98, 0x2000
	s_cselect_b32 s0, s0, 0x4000000
	s_lshl_b32 s2, s98, 15
	s_and_b32 s2, s2, 0x7c00000
	s_and_b32 s12, s98, 7
	s_lshl_b32 s12, s12, 19
	s_or_b32 s2, s2, s12
	s_lshl_b32 s12, s98, 4
	s_and_b32 s12, s12, 0x780
	s_or_b32 s2, s2, s12
	s_add_u32 s2, s2, s0
	s_add_u32 s0, s26, s2
	s_addc_u32 s1, s27, 0
	ds_write_b128 v242, v[0:3] offset:0
	ds_write_b128 v242, v[4:7] offset:128
	ds_write_b128 v242, v[8:11] offset:256
	ds_write_b128 v242, v[12:15] offset:384
	s_waitcnt lgkmcnt(0)
	s_barrier
	ds_read_b128 v[16:19], v243 offset:0
	ds_read_b128 v[20:23], v244 offset:1024
	ds_read_b128 v[24:27], v245 offset:2048
	ds_read_b128 v[28:31], v246 offset:3072
	s_waitcnt lgkmcnt(3)
	global_store_dwordx4 v236, v[16:19], s[0:1] nt
	s_waitcnt lgkmcnt(2)
	global_store_dwordx4 v237, v[20:23], s[0:1] nt
	s_waitcnt lgkmcnt(1)
	global_store_dwordx4 v238, v[24:27], s[0:1] nt
	s_waitcnt lgkmcnt(0)
	global_store_dwordx4 v239, v[28:31], s[0:1] nt
	v_xor_b32_e32 v242, 0x8000, v242
	v_xor_b32_e32 v243, 0x8000, v243
	v_xor_b32_e32 v244, 0x8000, v244
	v_xor_b32_e32 v245, 0x8000, v245
	v_xor_b32_e32 v246, 0x8000, v246
	s_mov_b32 s98, s101
	s_add_i32 s101, s101, vcc_lo
	s_cmp_lt_u32 s98, vcc_hi
	s_cbranch_scc1 .Lcv_ld_l0
	s_mov_b32 s16, 99
	s_branch .Lcv_ldskip_l0

.Lcv_ldskip_l0:
	s_cmp_lt_u32 s99, vcc_hi
	s_cbranch_scc0 .Lcv_done
	s_cmp_eq_u32 s16, 0
	s_cbranch_scc1 .Lcv_w40_f1
	s_cmp_eq_u32 s16, 99
	s_cbranch_scc1 .Lcv_w0_f1
	s_sub_u32 s16, s16, 1
	s_waitcnt vmcnt(32)
	s_branch .Lcv_wd_f1

.Lcv_wd_f1:
	v_pk_mul_f32 v[64:65], v[64:65], v[240:241]
	v_pk_mul_f32 v[66:67], v[66:67], v[240:241]
	v_pk_mul_f32 v[68:69], v[68:69], v[240:241]
	v_pk_mul_f32 v[70:71], v[70:71], v[240:241]
	v_pk_mul_f32 v[72:73], v[72:73], v[240:241]
	v_pk_mul_f32 v[74:75], v[74:75], v[240:241]
	v_pk_mul_f32 v[76:77], v[76:77], v[240:241]
	v_pk_mul_f32 v[78:79], v[78:79], v[240:241]
	v_pk_mul_f32 v[80:81], v[80:81], v[240:241]
	v_pk_mul_f32 v[82:83], v[82:83], v[240:241]
	v_pk_mul_f32 v[84:85], v[84:85], v[240:241]
	v_pk_mul_f32 v[86:87], v[86:87], v[240:241]
	v_pk_mul_f32 v[88:89], v[88:89], v[240:241]
	v_pk_mul_f32 v[90:91], v[90:91], v[240:241]
	v_pk_mul_f32 v[92:93], v[92:93], v[240:241]
	v_pk_mul_f32 v[94:95], v[94:95], v[240:241]
	v_pk_mul_f32 v[96:97], v[96:97], v[240:241]
	v_pk_mul_f32 v[98:99], v[98:99], v[240:241]
	v_pk_mul_f32 v[100:101], v[100:101], v[240:241]
	v_pk_mul_f32 v[102:103], v[102:103], v[240:241]
	v_pk_mul_f32 v[104:105], v[104:105], v[240:241]
	v_pk_mul_f32 v[106:107], v[106:107], v[240:241]
	v_pk_mul_f32 v[108:109], v[108:109], v[240:241]
	v_pk_mul_f32 v[110:111], v[110:111], v[240:241]
	v_pk_mul_f32 v[112:113], v[112:113], v[240:241]
	v_pk_mul_f32 v[114:115], v[114:115], v[240:241]
	v_pk_mul_f32 v[116:117], v[116:117], v[240:241]
	v_pk_mul_f32 v[118:119], v[118:119], v[240:241]
	v_pk_mul_f32 v[120:121], v[120:121], v[240:241]
	v_pk_mul_f32 v[122:123], v[122:123], v[240:241]
	v_pk_mul_f32 v[124:125], v[124:125], v[240:241]
	v_pk_mul_f32 v[126:127], v[126:127], v[240:241]
	v_cvt_pk_fp8_f32 v128, v64, v68
	v_cvt_pk_fp8_f32 v129, v65, v69
	v_cvt_pk_fp8_f32 v130, v66, v70
	v_cvt_pk_fp8_f32 v131, v67, v71
	v_cvt_pk_fp8_f32 v128, v72, v76 op_sel:[0,0,1]
	v_cvt_pk_fp8_f32 v129, v73, v77 op_sel:[0,0,1]
	v_cvt_pk_fp8_f32 v130, v74, v78 op_sel:[0,0,1]
	v_cvt_pk_fp8_f32 v131, v75, v79 op_sel:[0,0,1]
	v_cvt_pk_fp8_f32 v65, v80, v84
	v_cvt_pk_fp8_f32 v69, v81, v85
	v_cvt_pk_fp8_f32 v73, v82, v86
	v_cvt_pk_fp8_f32 v77, v83, v87
	v_cvt_pk_fp8_f32 v66, v96, v100
	v_cvt_pk_fp8_f32 v70, v97, v101
	v_cvt_pk_fp8_f32 v74, v98, v102
	v_cvt_pk_fp8_f32 v78, v99, v103
	v_cvt_pk_fp8_f32 v67, v112, v116
	v_cvt_pk_fp8_f32 v71, v113, v117
	v_cvt_pk_fp8_f32 v75, v114, v118
	v_cvt_pk_fp8_f32 v79, v115, v119
	v_cvt_pk_fp8_f32 v65, v88, v92 op_sel:[0,0,1]
	v_cvt_pk_fp8_f32 v69, v89, v93 op_sel:[0,0,1]
	v_cvt_pk_fp8_f32 v73, v90, v94 op_sel:[0,0,1]
	v_cvt_pk_fp8_f32 v77, v91, v95 op_sel:[0,0,1]
	v_cvt_pk_fp8_f32 v66, v104, v108 op_sel:[0,0,1]
	v_cvt_pk_fp8_f32 v70, v105, v109 op_sel:[0,0,1]
	v_cvt_pk_fp8_f32 v74, v106, v110 op_sel:[0,0,1]
	v_cvt_pk_fp8_f32 v78, v107, v111 op_sel:[0,0,1]
	v_cvt_pk_fp8_f32 v67, v120, v124 op_sel:[0,0,1]
	v_cvt_pk_fp8_f32 v71, v121, v125 op_sel:[0,0,1]
	v_cvt_pk_fp8_f32 v75, v122, v126 op_sel:[0,0,1]
	v_cvt_pk_fp8_f32 v79, v123, v127 op_sel:[0,0,1]
	v_mov_b32_e32 v64, v128
	v_mov_b32_e32 v68, v129
	v_mov_b32_e32 v72, v130
	v_mov_b32_e32 v76, v131
	s_cmp_lt_u32 s99, 0x1000
	s_mov_b32 s0, 0x24000000
	s_cselect_b32 s0, 0x14000000, s0
	s_cmp_lt_u32 s99, 0x2000
	s_cselect_b32 s0, s0, 0x4000000
	s_lshl_b32 s2, s99, 15
	s_and_b32 s2, s2, 0x7c00000
	s_and_b32 s12, s99, 7
	s_lshl_b32 s12, s12, 19
	s_or_b32 s2, s2, s12
	s_lshl_b32 s12, s99, 4
	s_and_b32 s12, s12, 0x780
	s_or_b32 s2, s2, s12
	s_add_u32 s2, s2, s0
	s_add_u32 s0, s26, s2
	s_addc_u32 s1, s27, 0
	ds_write_b128 v242, v[64:67] offset:0
	ds_write_b128 v242, v[68:71] offset:128
	ds_write_b128 v242, v[72:75] offset:256
	ds_write_b128 v242, v[76:79] offset:384
	s_waitcnt lgkmcnt(0)
	s_barrier
	ds_read_b128 v[80:83], v243 offset:0
	ds_read_b128 v[84:87], v244 offset:1024
	ds_read_b128 v[88:91], v245 offset:2048
	ds_read_b128 v[92:95], v246 offset:3072
	s_waitcnt lgkmcnt(3)
	global_store_dwordx4 v236, v[80:83], s[0:1] nt
	s_waitcnt lgkmcnt(2)
	global_store_dwordx4 v237, v[84:87], s[0:1] nt
	s_waitcnt lgkmcnt(1)
	global_store_dwordx4 v238, v[88:91], s[0:1] nt
	s_waitcnt lgkmcnt(0)
	global_store_dwordx4 v239, v[92:95], s[0:1] nt
	v_xor_b32_e32 v242, 0x8000, v242
	v_xor_b32_e32 v243, 0x8000, v243
	v_xor_b32_e32 v244, 0x8000, v244
	v_xor_b32_e32 v245, 0x8000, v245
	v_xor_b32_e32 v246, 0x8000, v246
	s_mov_b32 s99, s101
	s_add_i32 s101, s101, vcc_lo
	s_cmp_lt_u32 s99, vcc_hi
	s_cbranch_scc1 .Lcv_ld_l1
	s_mov_b32 s16, 99
	s_branch .Lcv_ldskip_l1

.Lcv_ldskip_l1:
	s_cmp_lt_u32 s100, vcc_hi
	s_cbranch_scc0 .Lcv_done
	s_cmp_eq_u32 s16, 0
	s_cbranch_scc1 .Lcv_w40_f2
	s_cmp_eq_u32 s16, 99
	s_cbranch_scc1 .Lcv_w0_f2
	s_sub_u32 s16, s16, 1
	s_waitcnt vmcnt(32)
	s_branch .Lcv_wd_f2

.Lcv_wd_f2:
	v_pk_mul_f32 v[136:137], v[136:137], v[240:241]
	v_pk_mul_f32 v[138:139], v[138:139], v[240:241]
	v_pk_mul_f32 v[140:141], v[140:141], v[240:241]
	v_pk_mul_f32 v[142:143], v[142:143], v[240:241]
	v_pk_mul_f32 v[144:145], v[144:145], v[240:241]
	v_pk_mul_f32 v[146:147], v[146:147], v[240:241]
	v_pk_mul_f32 v[148:149], v[148:149], v[240:241]
	v_pk_mul_f32 v[150:151], v[150:151], v[240:241]
	v_pk_mul_f32 v[152:153], v[152:153], v[240:241]
	v_pk_mul_f32 v[154:155], v[154:155], v[240:241]
	v_pk_mul_f32 v[156:157], v[156:157], v[240:241]
	v_pk_mul_f32 v[158:159], v[158:159], v[240:241]
	v_pk_mul_f32 v[160:161], v[160:161], v[240:241]
	v_pk_mul_f32 v[162:163], v[162:163], v[240:241]
	v_pk_mul_f32 v[164:165], v[164:165], v[240:241]
	v_pk_mul_f32 v[166:167], v[166:167], v[240:241]
	v_pk_mul_f32 v[168:169], v[168:169], v[240:241]
	v_pk_mul_f32 v[170:171], v[170:171], v[240:241]
	v_pk_mul_f32 v[172:173], v[172:173], v[240:241]
	v_pk_mul_f32 v[174:175], v[174:175], v[240:241]
	v_pk_mul_f32 v[184:185], v[184:185], v[240:241]
	v_pk_mul_f32 v[186:187], v[186:187], v[240:241]
	v_pk_mul_f32 v[188:189], v[188:189], v[240:241]
	v_pk_mul_f32 v[190:191], v[190:191], v[240:241]
	v_pk_mul_f32 v[192:193], v[192:193], v[240:241]
	v_pk_mul_f32 v[194:195], v[194:195], v[240:241]
	v_pk_mul_f32 v[196:197], v[196:197], v[240:241]
	v_pk_mul_f32 v[198:199], v[198:199], v[240:241]
	v_pk_mul_f32 v[200:201], v[200:201], v[240:241]
	v_pk_mul_f32 v[202:203], v[202:203], v[240:241]
	v_pk_mul_f32 v[204:205], v[204:205], v[240:241]
	v_pk_mul_f32 v[206:207], v[206:207], v[240:241]
	v_cvt_pk_fp8_f32 v128, v136, v140
	v_cvt_pk_fp8_f32 v129, v137, v141
	v_cvt_pk_fp8_f32 v130, v138, v142
	v_cvt_pk_fp8_f32 v131, v139, v143
	v_cvt_pk_fp8_f32 v128, v144, v148 op_sel:[0,0,1]
	v_cvt_pk_fp8_f32 v129, v145, v149 op_sel:[0,0,1]
	v_cvt_pk_fp8_f32 v130, v146, v150 op_sel:[0,0,1]
	v_cvt_pk_fp8_f32 v131, v147, v151 op_sel:[0,0,1]
	v_cvt_pk_fp8_f32 v137, v152, v156
	v_cvt_pk_fp8_f32 v141, v153, v157
	v_cvt_pk_fp8_f32 v145, v154, v158
	v_cvt_pk_fp8_f32 v149, v155, v159
	v_cvt_pk_fp8_f32 v138, v168, v172
	v_cvt_pk_fp8_f32 v142, v169, v173
	v_cvt_pk_fp8_f32 v146, v170, v174
	v_cvt_pk_fp8_f32 v150, v171, v175
	v_cvt_pk_fp8_f32 v139, v192, v196
	v_cvt_pk_fp8_f32 v143, v193, v197
	v_cvt_pk_fp8_f32 v147, v194, v198
	v_cvt_pk_fp8_f32 v151, v195, v199
	v_cvt_pk_fp8_f32 v137, v160, v164 op_sel:[0,0,1]
	v_cvt_pk_fp8_f32 v141, v161, v165 op_sel:[0,0,1]
	v_cvt_pk_fp8_f32 v145, v162, v166 op_sel:[0,0,1]
	v_cvt_pk_fp8_f32 v149, v163, v167 op_sel:[0,0,1]
	v_cvt_pk_fp8_f32 v138, v184, v188 op_sel:[0,0,1]
	v_cvt_pk_fp8_f32 v142, v185, v189 op_sel:[0,0,1]
	v_cvt_pk_fp8_f32 v146, v186, v190 op_sel:[0,0,1]
	v_cvt_pk_fp8_f32 v150, v187, v191 op_sel:[0,0,1]
	v_cvt_pk_fp8_f32 v139, v200, v204 op_sel:[0,0,1]
	v_cvt_pk_fp8_f32 v143, v201, v205 op_sel:[0,0,1]
	v_cvt_pk_fp8_f32 v147, v202, v206 op_sel:[0,0,1]
	v_cvt_pk_fp8_f32 v151, v203, v207 op_sel:[0,0,1]
	v_mov_b32_e32 v136, v128
	v_mov_b32_e32 v140, v129
	v_mov_b32_e32 v144, v130
	v_mov_b32_e32 v148, v131
	s_cmp_lt_u32 s100, 0x1000
	s_mov_b32 s0, 0x24000000
	s_cselect_b32 s0, 0x14000000, s0
	s_cmp_lt_u32 s100, 0x2000
	s_cselect_b32 s0, s0, 0x4000000
	s_lshl_b32 s2, s100, 15
	s_and_b32 s2, s2, 0x7c00000
	s_and_b32 s12, s100, 7
	s_lshl_b32 s12, s12, 19
	s_or_b32 s2, s2, s12
	s_lshl_b32 s12, s100, 4
	s_and_b32 s12, s12, 0x780
	s_or_b32 s2, s2, s12
	s_add_u32 s2, s2, s0
	s_add_u32 s0, s26, s2
	s_addc_u32 s1, s27, 0
	ds_write_b128 v242, v[136:139] offset:0
	ds_write_b128 v242, v[140:143] offset:128
	ds_write_b128 v242, v[144:147] offset:256
	ds_write_b128 v242, v[148:151] offset:384
	s_waitcnt lgkmcnt(0)
	s_barrier
	ds_read_b128 v[152:155], v243 offset:0
	ds_read_b128 v[156:159], v244 offset:1024
	ds_read_b128 v[160:163], v245 offset:2048
	ds_read_b128 v[164:167], v246 offset:3072
	s_waitcnt lgkmcnt(3)
	global_store_dwordx4 v236, v[152:155], s[0:1] nt
	s_waitcnt lgkmcnt(2)
	global_store_dwordx4 v237, v[156:159], s[0:1] nt
	s_waitcnt lgkmcnt(1)
	global_store_dwordx4 v238, v[160:163], s[0:1] nt
	s_waitcnt lgkmcnt(0)
	global_store_dwordx4 v239, v[164:167], s[0:1] nt
	v_xor_b32_e32 v242, 0x8000, v242
	v_xor_b32_e32 v243, 0x8000, v243
	v_xor_b32_e32 v244, 0x8000, v244
	v_xor_b32_e32 v245, 0x8000, v245
	v_xor_b32_e32 v246, 0x8000, v246
	s_mov_b32 s100, s101
	s_add_i32 s101, s101, vcc_lo
	s_cmp_lt_u32 s100, vcc_hi
	s_cbranch_scc1 .Lcv_ld_l2
	s_mov_b32 s16, 99
	s_branch .Lcv_ldskip_l2

.LBB0_2254:
	s_cmp_lt_i32 s92, 13
	s_cselect_b64 s[0:1], -1, 0
	s_cmp_gt_i32 s93, 12
	s_cselect_b64 s[2:3], -1, 0
	s_and_b64 s[0:1], s[0:1], s[2:3]
	v_cndmask_b32_e64 v0, 0, 1, s[0:1]
	v_cmp_ne_u32_e64 s[4:5], 1, v0
	s_andn2_b64 vcc, exec, s[0:1]
	v_mbcnt_lo_u32_b32 v0, -1, 0
	v_mbcnt_hi_u32_b32 v0, -1, v0
	s_cbranch_vccnz .LBB0_2288
	v_mbcnt_lo_u32_b32 v0, -1, 0
	v_mbcnt_hi_u32_b32 v0, -1, v0
	v_add_u32_e32 v0, s52, v0
	v_lshlrev_b32_e32 v0, 2, v0
	s_add_u32 s6, s26, 0xf00000
	s_addc_u32 s7, s27, 0
	global_load_dword v1, v0, s[6:7]
	global_load_dword v2, v0, s[6:7] offset:2048
	v_mov_b32_e32 v3, 0x1000
	global_load_dword v3, v3, s[6:7]
	s_load_dwordx2 s[98:99], s[90:91], 0xb0
	s_load_dwordx2 s[100:101], s[90:91], 0xc0
	s_mov_b32 s32, 0x22000
	v_add_u32_e32 v0, 0x20000, v0
	s_waitcnt vmcnt(0)
	ds_write_b32 v0, v1
	ds_write_b32 v0, v2 offset:2048
	v_mov_b32_e32 v4, 0x21100
	ds_write_b32 v4, v3
	s_waitcnt lgkmcnt(0)
	s_barrier
	s_mov_b32 s0, 16
	s_waitcnt lgkmcnt(0)
	v_mov_b32_e32 v1, 0xf01000
	v_mbcnt_lo_u32_b32 v0, -1, 0
	v_mbcnt_hi_u32_b32 v0, -1, v0
	global_load_dword v2, v1, s[26:27]
	s_ashr_i32 s95, s94, 31
	s_add_u32 s8, s26, 0xf01000
	v_add_u32_e32 v1, s52, v0
	s_addc_u32 s9, s27, 0
	v_readfirstlane_b32 s16, v1
	s_waitcnt vmcnt(0)
	v_ashrrev_i32_e32 v3, 31, v2
	v_readfirstlane_b32 s2, v2
	v_lshlrev_b64 v[2:3], 4, v[2:3]
	v_cmp_ge_i64_e32 vcc, s[94:95], v[2:3]
	s_cbranch_vccnz .LBB0_2288
	s_lshr_b32 s1, s95, 29
	s_add_i32 s1, s94, s1
	s_ashr_i32 s3, s1, 3
	s_and_b32 s1, s1, -8
	s_sub_i32 s1, s94, s1
	v_mov_b32_e32 v2, s1
	v_alignbit_b32 v2, s2, v2, 31
	s_nop 0
	v_readfirstlane_b32 s6, v2
	s_mul_i32 s1, s6, s1
	s_add_i32 s6, s1, s3
	s_ashr_i32 s1, s6, 31
	s_lshr_b32 s1, s1, 25
	s_add_i32 s7, s6, s1
	s_ashr_i32 s1, s7, 7
	s_lshl_b32 s1, s1, 3
	s_sub_i32 s3, s2, s1
	s_and_b32 s2, s7, 0xffffff80
	s_sub_i32 s2, s6, s2
	s_cmp_lt_i32 s3, 8
	s_cbranch_scc0 .LBB0_2258
	s_abs_i32 s6, s3
	v_cvt_f32_u32_e32 v2, s6
	s_sub_i32 s11, 0, s6
	s_abs_i32 s10, s2
	s_xor_b32 s7, s2, s3
	v_rcp_iflag_f32_e32 v2, v2
	s_ashr_i32 s7, s7, 31
	v_mul_f32_e32 v2, 0x4f7ffffe, v2
	v_cvt_u32_f32_e32 v2, v2
	s_nop 0
	v_readfirstlane_b32 s12, v2
	s_mul_i32 s11, s11, s12
	s_mul_hi_u32 s11, s12, s11
	s_add_i32 s12, s12, s11
	s_mul_hi_u32 s11, s10, s12
	s_mul_i32 s12, s11, s6
	s_sub_i32 s10, s10, s12
	s_add_i32 s13, s11, 1
	s_sub_i32 s12, s10, s6
	s_cmp_ge_u32 s10, s6
	s_cselect_b32 s11, s13, s11
	s_cselect_b32 s10, s12, s10
	s_add_i32 s12, s11, 1
	s_cmp_ge_u32 s10, s6
	s_cselect_b32 s6, s12, s11
	s_xor_b32 s6, s6, s7
	s_sub_i32 s6, s6, s7
	s_mul_i32 s3, s6, s3
	s_sub_i32 s3, s2, s3
	s_add_i32 s14, s3, s1
	s_cbranch_execz .LBB0_2259
	s_branch .LBB0_2260

.LBB0_2265:
	s_mov_b32 s6, s71
	s_add_i32 s71, s71, 1
	s_cmp_gt_u32 s6, 0x3ffffffe
	s_cbranch_scc1 .LBB0_2272
	v_mov_b32_e32 v0, 0x21100
	ds_read_b32 v0, v0
	s_load_dword s30, s[90:91], 0x100
	s_mul_i32 s6, s71, s72
	s_waitcnt lgkmcnt(0)
	s_mul_hi_u32 s7, s71, s30
	s_mul_i32 s30, s71, s30
	s_add_i32 s7, s7, s6
	s_add_u32 s6, s30, s94
	s_addc_u32 s7, s7, s95
	s_waitcnt lgkmcnt(0)
	v_ashrrev_i32_e32 v1, 31, v0
	v_readfirstlane_b32 s30, v0
	v_lshlrev_b64 v[0:1], 4, v[0:1]
	v_cmp_ge_i64_e32 vcc, s[6:7], v[0:1]
	s_cbranch_vccnz .LBB0_2273
	s_ashr_i32 s7, s6, 31
	s_lshr_b32 s7, s7, 29
	s_add_i32 s7, s6, s7
	s_ashr_i32 s22, s7, 3
	s_and_b32 s7, s7, -8
	s_sub_i32 s6, s6, s7
	v_mov_b32_e32 v0, s6
	v_alignbit_b32 v0, s30, v0, 31
	s_nop 0
	v_readfirstlane_b32 s7, v0
	s_mul_i32 s6, s7, s6
	s_add_i32 s6, s6, s22
	s_ashr_i32 s7, s6, 31
	s_lshr_b32 s7, s7, 25
	s_add_i32 s22, s6, s7
	s_ashr_i32 s7, s22, 7
	s_lshl_b32 s7, s7, 3
	s_and_b32 s22, s22, 0xffffff80
	s_sub_i32 s29, s30, s7
	s_sub_i32 s28, s6, s22
	s_cmp_lt_i32 s29, 8
	s_mov_b64 s[22:23], -1
	s_cbranch_scc0 .LBB0_2269
	s_abs_i32 s6, s29
	v_cvt_f32_u32_e32 v0, s6
	s_sub_i32 s30, 0, s6
	s_abs_i32 s23, s28
	s_xor_b32 s22, s28, s29
	v_rcp_iflag_f32_e32 v0, v0
	s_ashr_i32 s22, s22, 31
	v_mul_f32_e32 v0, 0x4f7ffffe, v0
	v_cvt_u32_f32_e32 v0, v0
	s_nop 0
	v_readfirstlane_b32 s31, v0
	s_mul_i32 s30, s30, s31
	s_mul_hi_u32 s30, s31, s30
	s_add_i32 s31, s31, s30
	s_mul_hi_u32 s30, s23, s31
	s_mul_i32 s31, s30, s6
	s_sub_i32 s23, s23, s31
	s_add_i32 s34, s30, 1
	s_sub_i32 s31, s23, s6
	s_cmp_ge_u32 s23, s6
	s_cselect_b32 s30, s34, s30
	s_cselect_b32 s23, s31, s23
	s_add_i32 s31, s30, 1
	s_cmp_ge_u32 s23, s6
	s_cselect_b32 s6, s31, s30
	s_xor_b32 s6, s6, s22
	s_sub_i32 s6, s6, s22
	s_mul_i32 s22, s6, s29
	s_sub_i32 s22, s28, s22
	s_add_i32 s34, s22, s7
	s_mov_b64 s[22:23], 0

.Lgx_skip:
	s_xor_b32 s32, s32, 0x400
	v_mbcnt_lo_u32_b32 v255, -1, 0
	v_mbcnt_hi_u32_b32 v255, -1, v255
	v_lshlrev_b32_e32 v255, 2, v255
	v_lshl_add_u32 v255, v164, 13, v255
	s_lshl_b32 s89, s46, 2
	v_add_u32_e32 v255, s89, v255
	s_mov_b32 m0, s32
	s_nop 0
	global_load_lds_dword v255, s[98:99]
	global_load_lds_dword v255, s[98:99] offset:256
	s_add_i32 m0, s32, 0x200
	s_nop 0
	global_load_lds_dword v255, s[100:101]
	global_load_lds_dword v255, s[100:101] offset:256
	v_mov_b32_e32 v33, v32
	v_mov_b32_e32 v34, v32
	v_mov_b32_e32 v35, v32
	v_mov_b32_e32 v56, v32
	v_mov_b32_e32 v57, v32
	v_mov_b32_e32 v58, v32
	v_mov_b32_e32 v59, v32
	v_mov_b32_e32 v48, v32
	v_mov_b32_e32 v49, v32
	v_mov_b32_e32 v50, v32
	v_mov_b32_e32 v51, v32
	v_mov_b32_e32 v40, v32
	v_mov_b32_e32 v41, v32
	v_mov_b32_e32 v42, v32
	v_mov_b32_e32 v43, v32
	v_mov_b32_e32 v64, v32
	v_mov_b32_e32 v65, v32
	v_mov_b32_e32 v66, v32
	v_mov_b32_e32 v67, v32
	v_mov_b32_e32 v72, v32
	v_mov_b32_e32 v73, v32
	v_mov_b32_e32 v74, v32
	v_mov_b32_e32 v75, v32
	v_mov_b32_e32 v80, v32
	v_mov_b32_e32 v81, v32
	v_mov_b32_e32 v82, v32
	v_mov_b32_e32 v83, v32
	v_mov_b32_e32 v88, v32
	v_mov_b32_e32 v89, v32
	v_mov_b32_e32 v90, v32
	v_mov_b32_e32 v91, v32
	v_mov_b32_e32 v36, v32
	v_mov_b32_e32 v37, v32
	v_mov_b32_e32 v38, v32
	v_mov_b32_e32 v39, v32
	v_mov_b32_e32 v60, v32
	v_mov_b32_e32 v61, v32
	v_mov_b32_e32 v62, v32
	v_mov_b32_e32 v63, v32
	v_mov_b32_e32 v52, v32
	v_mov_b32_e32 v53, v32
	v_mov_b32_e32 v54, v32
	v_mov_b32_e32 v55, v32
	v_mov_b32_e32 v44, v32
	v_mov_b32_e32 v45, v32
	v_mov_b32_e32 v46, v32
	v_mov_b32_e32 v47, v32
	v_mov_b32_e32 v68, v32
	v_mov_b32_e32 v69, v32
	v_mov_b32_e32 v70, v32
	v_mov_b32_e32 v71, v32
	v_mov_b32_e32 v76, v32
	v_mov_b32_e32 v77, v32
	v_mov_b32_e32 v78, v32
	v_mov_b32_e32 v79, v32
	v_mov_b32_e32 v84, v32
	v_mov_b32_e32 v85, v32
	v_mov_b32_e32 v86, v32
	v_mov_b32_e32 v87, v32
	v_mov_b32_e32 v92, v32
	v_mov_b32_e32 v93, v32
	v_mov_b32_e32 v94, v32
	v_mov_b32_e32 v95, v32
	v_mov_b32_e32 v96, v32
	v_mov_b32_e32 v97, v32
	v_mov_b32_e32 v98, v32
	v_mov_b32_e32 v99, v32
	v_mov_b32_e32 v104, v32
	v_mov_b32_e32 v105, v32
	v_mov_b32_e32 v106, v32
	v_mov_b32_e32 v107, v32
	v_mov_b32_e32 v112, v32
	v_mov_b32_e32 v113, v32
	v_mov_b32_e32 v114, v32
	v_mov_b32_e32 v115, v32
	v_mov_b32_e32 v120, v32
	v_mov_b32_e32 v121, v32
	v_mov_b32_e32 v122, v32
	v_mov_b32_e32 v123, v32
	v_mov_b32_e32 v128, v32
	v_mov_b32_e32 v129, v32
	v_mov_b32_e32 v130, v32
	v_mov_b32_e32 v131, v32
	v_mov_b32_e32 v136, v32
	v_mov_b32_e32 v137, v32
	v_mov_b32_e32 v138, v32
	v_mov_b32_e32 v139, v32
	v_mov_b32_e32 v144, v32
	v_mov_b32_e32 v145, v32
	v_mov_b32_e32 v146, v32
	v_mov_b32_e32 v147, v32
	v_mov_b32_e32 v152, v32
	v_mov_b32_e32 v153, v32
	v_mov_b32_e32 v154, v32
	v_mov_b32_e32 v155, v32
	v_mov_b32_e32 v100, v32
	v_mov_b32_e32 v101, v32
	v_mov_b32_e32 v102, v32
	v_mov_b32_e32 v103, v32
	v_mov_b32_e32 v108, v32
	v_mov_b32_e32 v109, v32
	v_mov_b32_e32 v110, v32
	v_mov_b32_e32 v111, v32
	v_mov_b32_e32 v116, v32
	v_mov_b32_e32 v117, v32
	v_mov_b32_e32 v118, v32
	v_mov_b32_e32 v119, v32
	v_mov_b32_e32 v124, v32
	v_mov_b32_e32 v125, v32
	v_mov_b32_e32 v126, v32
	v_mov_b32_e32 v127, v32
	v_mov_b32_e32 v132, v32
	v_mov_b32_e32 v133, v32
	v_mov_b32_e32 v134, v32
	v_mov_b32_e32 v135, v32
	v_mov_b32_e32 v140, v32
	v_mov_b32_e32 v141, v32
	v_mov_b32_e32 v142, v32
	v_mov_b32_e32 v143, v32
	v_mov_b32_e32 v148, v32
	v_mov_b32_e32 v149, v32
	v_mov_b32_e32 v150, v32
	v_mov_b32_e32 v151, v32
	v_mov_b32_e32 v156, v32
	v_mov_b32_e32 v157, v32
	v_mov_b32_e32 v158, v32
	v_mov_b32_e32 v159, v32
	s_branch .LBB0_2279

.LBB0_2284:
	v_ashrrev_i32_e32 v165, 31, v164
	v_mov_b32_e32 v20, v179
	v_mov_b32_e32 v18, v181
	v_lshlrev_b64 v[0:1], 13, v[164:165]
	s_ashr_i32 s47, s46, 31
	s_waitcnt lgkmcnt(0)
	s_lshl_b64 s[46:47], s[46:47], 2
	v_ashrrev_i32_e32 v19, 31, v18
	v_lshlrev_b32_e32 v16, 2, v181
	v_add_u32_e32 v16, s32, v16
	ds_read_b128 v[12:15], v16
	ds_read_b128 v[4:7], v16 offset:16
	ds_read_b128 v[8:11], v16 offset:512
	ds_read_b128 v[0:3], v16 offset:528
	v_bfe_u32 v21, v18, 3, 1
	v_lshl_add_u32 v20, v21, 4, v20
	v_lshlrev_b32_e32 v22, 3, v21
	v_ashrrev_i32_e32 v21, 31, v20
	v_lshlrev_b64 v[20:21], 11, v[20:21]
	v_sub_co_u32_e32 v22, vcc, 0, v22
	v_lshl_add_u64 v[20:21], s[44:45], 0, v[20:21]
	s_nop 0
	v_subb_co_u32_e64 v23, s[46:47], 0, 0, vcc
	v_lshl_add_u64 v[18:19], v[20:21], 0, v[18:19]
	v_lshl_add_u64 v[20:21], v[18:19], 0, v[22:23]
	v_mov_b32_e32 v17, 0
	v_mov_b32_e32 v16, 0
	s_mov_b32 s44, 0x10000
	s_waitcnt lgkmcnt(0)
	v_pk_fma_f32 v[24:25], v[158:159], s[18:19], v[14:15] op_sel_hi:[1,0,1]
	v_pk_fma_f32 v[26:27], v[154:155], s[18:19], v[10:11] op_sel_hi:[1,0,1]
	v_pk_fma_f32 v[28:29], v[148:149], s[18:19], v[4:5] op_sel_hi:[1,0,1]
	v_med3_f32 v26, v26, s76, v185
	v_med3_f32 v27, v27, s76, v185
	v_min_f32_e32 v28, 0x40e00000, v28
	v_min_f32_e32 v29, 0x40e00000, v29
	v_pk_fma_f32 v[18:19], v[156:157], s[18:19], v[12:13] op_sel_hi:[1,0,1]
	v_pk_fma_f32 v[22:23], v[152:153], s[18:19], v[8:9] op_sel_hi:[1,0,1]
	v_min_f32_e32 v24, 0x40e00000, v24
	v_min_f32_e32 v25, 0x40e00000, v25
	v_pk_fma_f32 v[26:27], v[26:27], 4.0, 4.0 op_sel_hi:[1,0,0]
	v_pk_mul_f32 v[152:153], v[28:29], s[20:21] op_sel_hi:[1,0]
	v_pk_fma_f32 v[30:31], v[144:145], s[18:19], v[0:1] op_sel_hi:[1,0,1]
	v_pk_fma_f32 v[144:145], v[150:151], s[18:19], v[6:7] op_sel_hi:[1,0,1]
	v_min_f32_e32 v18, 0x40e00000, v18
	v_min_f32_e32 v19, 0x40e00000, v19
	v_pk_mul_f32 v[150:151], v[24:25], s[20:21] op_sel_hi:[1,0]
	v_pk_mul_f32 v[24:25], v[24:25], v[26:27]
	v_exp_f32_e32 v26, v152
	v_exp_f32_e32 v27, v153
	v_pk_mul_f32 v[148:149], v[18:19], s[20:21] op_sel_hi:[1,0]
	v_med3_f32 v22, v22, s76, v185
	v_med3_f32 v23, v23, s76, v185
	v_med3_f32 v30, v30, s76, v185
	v_med3_f32 v31, v31, s76, v185
	v_min_f32_e32 v144, 0x40e00000, v144
	v_min_f32_e32 v145, 0x40e00000, v145
	v_exp_f32_e32 v148, v148
	v_exp_f32_e32 v149, v149
	v_pk_fma_f32 v[22:23], v[22:23], 4.0, 4.0 op_sel_hi:[1,0,0]
	v_pk_fma_f32 v[30:31], v[30:31], 4.0, 4.0 op_sel_hi:[1,0,0]
	v_pk_mul_f32 v[154:155], v[144:145], s[20:21] op_sel_hi:[1,0]
	v_pk_mul_f32 v[18:19], v[18:19], v[22:23]
	v_exp_f32_e32 v22, v150
	v_exp_f32_e32 v23, v151
	v_pk_mul_f32 v[28:29], v[28:29], v[30:31]
	v_exp_f32_e32 v30, v154
	v_exp_f32_e32 v31, v155
	v_pk_add_f32 v[26:27], v[26:27], 1.0 op_sel_hi:[1,0]
	v_pk_add_f32 v[148:149], v[148:149], 1.0 op_sel_hi:[1,0]
	v_rcp_f32_e32 v26, v26
	v_rcp_f32_e32 v27, v27
	v_pk_fma_f32 v[146:147], v[146:147], s[18:19], v[2:3] op_sel_hi:[1,0,1]
	v_pk_fma_f32 v[140:141], v[140:141], s[18:19], v[12:13] op_sel_hi:[1,0,1]
	v_rcp_f32_e32 v148, v148
	v_rcp_f32_e32 v149, v149
	v_med3_f32 v146, v146, s76, v185
	v_med3_f32 v147, v147, s76, v185
	v_min_f32_e32 v140, 0x40e00000, v140
	v_min_f32_e32 v141, 0x40e00000, v141
	v_pk_add_f32 v[22:23], v[22:23], 1.0 op_sel_hi:[1,0]
	v_pk_add_f32 v[30:31], v[30:31], 1.0 op_sel_hi:[1,0]
	v_pk_fma_f32 v[146:147], v[146:147], 4.0, 4.0 op_sel_hi:[1,0,0]
	v_pk_mul_f32 v[156:157], v[140:141], s[20:21] op_sel_hi:[1,0]
	v_rcp_f32_e32 v22, v22
	v_rcp_f32_e32 v23, v23
	v_rcp_f32_e32 v30, v30
	v_rcp_f32_e32 v31, v31
	v_pk_mul_f32 v[26:27], v[28:29], v[26:27]
	v_pk_mul_f32 v[144:145], v[144:145], v[146:147]
	v_exp_f32_e32 v146, v156
	v_exp_f32_e32 v147, v157
	v_cvt_pk_fp8_f32 v17, v26, v27
	v_pk_mul_f32 v[18:19], v[18:19], v[148:149]
	v_pk_fma_f32 v[136:137], v[136:137], s[18:19], v[8:9] op_sel_hi:[1,0,1]
	v_cvt_pk_fp8_f32 v16, v18, v19
	v_pk_mul_f32 v[18:19], v[24:25], v[22:23]
	v_pk_mul_f32 v[22:23], v[144:145], v[30:31]
	v_pk_fma_f32 v[26:27], v[138:139], s[18:19], v[10:11] op_sel_hi:[1,0,1]
	v_cvt_pk_fp8_f32 v17, v22, v23 op_sel:[0,0,1]
	v_pk_add_f32 v[22:23], v[146:147], 1.0 op_sel_hi:[1,0]
	v_cvt_pk_fp8_f32 v16, v18, v19 op_sel:[0,0,1]
	v_rcp_f32_e32 v22, v22
	v_rcp_f32_e32 v23, v23
	v_med3_f32 v18, v136, s76, v185
	v_med3_f32 v19, v137, s76, v185
	v_pk_fma_f32 v[18:19], v[18:19], 4.0, 4.0 op_sel_hi:[1,0,0]
	v_med3_f32 v26, v26, s76, v185
	v_pk_mul_f32 v[18:19], v[140:141], v[18:19]
	v_med3_f32 v27, v27, s76, v185
	v_pk_mul_f32 v[22:23], v[18:19], v[22:23]
	v_pk_fma_f32 v[18:19], v[142:143], s[18:19], v[14:15] op_sel_hi:[1,0,1]
	v_pk_fma_f32 v[26:27], v[26:27], 4.0, 4.0 op_sel_hi:[1,0,0]
	v_min_f32_e32 v18, 0x40e00000, v18
	v_min_f32_e32 v19, 0x40e00000, v19
	v_pk_mul_f32 v[24:25], v[18:19], s[20:21] op_sel_hi:[1,0]
	v_pk_mul_f32 v[18:19], v[18:19], v[26:27]
	v_exp_f32_e32 v24, v24
	v_exp_f32_e32 v25, v25
	v_pk_fma_f32 v[26:27], v[132:133], s[18:19], v[4:5] op_sel_hi:[1,0,1]
	v_pk_fma_f32 v[30:31], v[130:131], s[18:19], v[2:3] op_sel_hi:[1,0,1]
	v_min_f32_e32 v26, 0x40e00000, v26
	v_min_f32_e32 v27, 0x40e00000, v27
	v_pk_mul_f32 v[28:29], v[26:27], s[20:21] op_sel_hi:[1,0]
	v_pk_add_f32 v[24:25], v[24:25], 1.0 op_sel_hi:[1,0]
	v_exp_f32_e32 v28, v28
	v_exp_f32_e32 v29, v29
	v_rcp_f32_e32 v24, v24
	v_rcp_f32_e32 v25, v25
	v_med3_f32 v30, v30, s76, v185
	v_pk_add_f32 v[28:29], v[28:29], 1.0 op_sel_hi:[1,0]
	v_med3_f32 v31, v31, s76, v185
	v_pk_mul_f32 v[24:25], v[18:19], v[24:25]
	v_pk_fma_f32 v[18:19], v[128:129], s[18:19], v[0:1] op_sel_hi:[1,0,1]
	v_rcp_f32_e32 v28, v28
	v_rcp_f32_e32 v29, v29
	v_med3_f32 v18, v18, s76, v185
	v_med3_f32 v19, v19, s76, v185
	v_pk_fma_f32 v[18:19], v[18:19], 4.0, 4.0 op_sel_hi:[1,0,0]
	v_pk_fma_f32 v[30:31], v[30:31], 4.0, 4.0 op_sel_hi:[1,0,0]
	v_pk_mul_f32 v[18:19], v[26:27], v[18:19]
	s_nop 0
	v_pk_mul_f32 v[26:27], v[18:19], v[28:29]
	v_pk_fma_f32 v[18:19], v[134:135], s[18:19], v[6:7] op_sel_hi:[1,0,1]
	s_nop 0
	v_min_f32_e32 v28, 0x40e00000, v18
	v_min_f32_e32 v29, 0x40e00000, v19
	v_pk_mul_f32 v[18:19], v[28:29], s[20:21] op_sel_hi:[1,0]
	s_nop 0
	v_exp_f32_e32 v18, v18
	v_exp_f32_e32 v19, v19
	s_nop 0
	v_pk_add_f32 v[18:19], v[18:19], 1.0 op_sel_hi:[1,0]
	s_nop 0
	v_rcp_f32_e32 v128, v18
	v_rcp_f32_e32 v129, v19
	v_mov_b32_e32 v19, 0
	v_cvt_pk_fp8_f32 v19, v26, v27
	v_mov_b32_e32 v18, 0
	v_cvt_pk_fp8_f32 v18, v22, v23
	v_pk_mul_f32 v[22:23], v[28:29], v[30:31]
	v_pk_fma_f32 v[28:29], v[114:115], s[18:19], v[2:3] op_sel_hi:[1,0,1]
	v_pk_mul_f32 v[22:23], v[22:23], v[128:129]
	v_cvt_pk_fp8_f32 v18, v24, v25 op_sel:[0,0,1]
	v_cvt_pk_fp8_f32 v19, v22, v23 op_sel:[0,0,1]
	v_pk_fma_f32 v[22:23], v[124:125], s[18:19], v[12:13] op_sel_hi:[1,0,1]
	v_med3_f32 v28, v28, s76, v185
	v_min_f32_e32 v22, 0x40e00000, v22
	v_min_f32_e32 v23, 0x40e00000, v23
	v_pk_mul_f32 v[24:25], v[22:23], s[20:21] op_sel_hi:[1,0]
	v_permlane16_swap_b32_e32 v16, v18
	v_exp_f32_e32 v24, v24
	v_exp_f32_e32 v25, v25
	v_permlane16_swap_b32_e32 v17, v19
	global_store_dwordx4 v[20:21], v[16:19], off
	v_med3_f32 v29, v29, s76, v185
	s_nop 0
	v_pk_add_f32 v[18:19], v[24:25], 1.0 op_sel_hi:[1,0]
	v_pk_fma_f32 v[16:17], v[120:121], s[18:19], v[8:9] op_sel_hi:[1,0,1]
	v_rcp_f32_e32 v18, v18
	v_rcp_f32_e32 v19, v19
	v_med3_f32 v16, v16, s76, v185
	v_med3_f32 v17, v17, s76, v185
	v_pk_fma_f32 v[16:17], v[16:17], 4.0, 4.0 op_sel_hi:[1,0,0]
	v_pk_fma_f32 v[24:25], v[122:123], s[18:19], v[10:11] op_sel_hi:[1,0,1]
	v_pk_mul_f32 v[16:17], v[22:23], v[16:17]
	v_med3_f32 v24, v24, s76, v185
	v_pk_mul_f32 v[18:19], v[16:17], v[18:19]
	v_pk_fma_f32 v[16:17], v[126:127], s[18:19], v[14:15] op_sel_hi:[1,0,1]
	v_med3_f32 v25, v25, s76, v185
	v_min_f32_e32 v16, 0x40e00000, v16
	v_min_f32_e32 v17, 0x40e00000, v17
	v_pk_mul_f32 v[22:23], v[16:17], s[20:21] op_sel_hi:[1,0]
	v_pk_fma_f32 v[24:25], v[24:25], 4.0, 4.0 op_sel_hi:[1,0,0]
	v_exp_f32_e32 v22, v22
	v_exp_f32_e32 v23, v23
	v_pk_mul_f32 v[16:17], v[16:17], v[24:25]
	v_pk_fma_f32 v[24:25], v[116:117], s[18:19], v[4:5] op_sel_hi:[1,0,1]
	v_pk_add_f32 v[22:23], v[22:23], 1.0 op_sel_hi:[1,0]
	v_min_f32_e32 v24, 0x40e00000, v24
	v_min_f32_e32 v25, 0x40e00000, v25
	v_pk_mul_f32 v[26:27], v[24:25], s[20:21] op_sel_hi:[1,0]
	v_rcp_f32_e32 v22, v22
	v_exp_f32_e32 v26, v26
	v_exp_f32_e32 v27, v27
	v_rcp_f32_e32 v23, v23
	v_pk_add_f32 v[26:27], v[26:27], 1.0 op_sel_hi:[1,0]
	v_pk_mul_f32 v[22:23], v[16:17], v[22:23]
	v_pk_fma_f32 v[16:17], v[112:113], s[18:19], v[0:1] op_sel_hi:[1,0,1]
	v_rcp_f32_e32 v26, v26
	v_rcp_f32_e32 v27, v27
	v_med3_f32 v16, v16, s76, v185
	v_med3_f32 v17, v17, s76, v185
	v_pk_fma_f32 v[16:17], v[16:17], 4.0, 4.0 op_sel_hi:[1,0,0]
	s_nop 0
	v_pk_mul_f32 v[16:17], v[24:25], v[16:17]
	s_nop 0
	v_pk_mul_f32 v[24:25], v[16:17], v[26:27]
	v_pk_fma_f32 v[16:17], v[118:119], s[18:19], v[6:7] op_sel_hi:[1,0,1]
	s_nop 0
	v_min_f32_e32 v26, 0x40e00000, v16
	v_min_f32_e32 v27, 0x40e00000, v17
	v_pk_mul_f32 v[16:17], v[26:27], s[20:21] op_sel_hi:[1,0]
	s_nop 0
	v_exp_f32_e32 v16, v16
	v_exp_f32_e32 v17, v17
	s_nop 0
	v_pk_add_f32 v[16:17], v[16:17], 1.0 op_sel_hi:[1,0]
	s_nop 0
	v_rcp_f32_e32 v30, v16
	v_mov_b32_e32 v16, 0
	v_cvt_pk_fp8_f32 v16, v18, v19
	v_rcp_f32_e32 v31, v17
	v_mov_b32_e32 v17, 0
	v_cvt_pk_fp8_f32 v17, v24, v25
	v_cvt_pk_fp8_f32 v16, v22, v23 op_sel:[0,0,1]
	v_pk_fma_f32 v[22:23], v[108:109], s[18:19], v[12:13] op_sel_hi:[1,0,1]
	v_pk_fma_f32 v[18:19], v[28:29], 4.0, 4.0 op_sel_hi:[1,0,0]
	v_min_f32_e32 v22, 0x40e00000, v22
	v_min_f32_e32 v23, 0x40e00000, v23
	v_pk_mul_f32 v[24:25], v[22:23], s[20:21] op_sel_hi:[1,0]
	v_pk_mul_f32 v[18:19], v[26:27], v[18:19]
	v_exp_f32_e32 v24, v24
	v_exp_f32_e32 v25, v25
	v_pk_mul_f32 v[18:19], v[18:19], v[30:31]
	v_pk_fma_f32 v[26:27], v[106:107], s[18:19], v[10:11] op_sel_hi:[1,0,1]
	v_cvt_pk_fp8_f32 v17, v18, v19 op_sel:[0,0,1]
	v_pk_add_f32 v[24:25], v[24:25], 1.0 op_sel_hi:[1,0]
	v_pk_fma_f32 v[18:19], v[104:105], s[18:19], v[8:9] op_sel_hi:[1,0,1]
	v_rcp_f32_e32 v24, v24
	v_rcp_f32_e32 v25, v25
	v_med3_f32 v18, v18, s76, v185
	v_med3_f32 v19, v19, s76, v185
	v_pk_fma_f32 v[18:19], v[18:19], 4.0, 4.0 op_sel_hi:[1,0,0]
	v_med3_f32 v26, v26, s76, v185
	v_pk_mul_f32 v[18:19], v[22:23], v[18:19]
	v_med3_f32 v27, v27, s76, v185
	v_pk_mul_f32 v[22:23], v[18:19], v[24:25]
	v_pk_fma_f32 v[18:19], v[110:111], s[18:19], v[14:15] op_sel_hi:[1,0,1]
	v_pk_fma_f32 v[26:27], v[26:27], 4.0, 4.0 op_sel_hi:[1,0,0]
	v_min_f32_e32 v18, 0x40e00000, v18
	v_min_f32_e32 v19, 0x40e00000, v19
	v_pk_mul_f32 v[24:25], v[18:19], s[20:21] op_sel_hi:[1,0]
	v_pk_mul_f32 v[18:19], v[18:19], v[26:27]
	v_exp_f32_e32 v24, v24
	v_exp_f32_e32 v25, v25
	v_pk_fma_f32 v[26:27], v[100:101], s[18:19], v[4:5] op_sel_hi:[1,0,1]
	v_pk_fma_f32 v[30:31], v[98:99], s[18:19], v[2:3] op_sel_hi:[1,0,1]
	v_min_f32_e32 v26, 0x40e00000, v26
	v_min_f32_e32 v27, 0x40e00000, v27
	v_pk_mul_f32 v[28:29], v[26:27], s[20:21] op_sel_hi:[1,0]
	v_pk_add_f32 v[24:25], v[24:25], 1.0 op_sel_hi:[1,0]
	v_exp_f32_e32 v28, v28
	v_exp_f32_e32 v29, v29
	v_rcp_f32_e32 v24, v24
	v_rcp_f32_e32 v25, v25
	v_med3_f32 v30, v30, s76, v185
	v_pk_add_f32 v[28:29], v[28:29], 1.0 op_sel_hi:[1,0]
	v_med3_f32 v31, v31, s76, v185
	v_pk_mul_f32 v[24:25], v[18:19], v[24:25]
	v_pk_fma_f32 v[18:19], v[96:97], s[18:19], v[0:1] op_sel_hi:[1,0,1]
	v_rcp_f32_e32 v28, v28
	v_rcp_f32_e32 v29, v29
	v_med3_f32 v18, v18, s76, v185
	v_med3_f32 v19, v19, s76, v185
	v_pk_fma_f32 v[18:19], v[18:19], 4.0, 4.0 op_sel_hi:[1,0,0]
	v_pk_fma_f32 v[30:31], v[30:31], 4.0, 4.0 op_sel_hi:[1,0,0]
	v_pk_mul_f32 v[18:19], v[26:27], v[18:19]
	s_nop 0
	v_pk_mul_f32 v[26:27], v[18:19], v[28:29]
	v_pk_fma_f32 v[18:19], v[102:103], s[18:19], v[6:7] op_sel_hi:[1,0,1]
	s_nop 0
	v_min_f32_e32 v28, 0x40e00000, v18
	v_min_f32_e32 v29, 0x40e00000, v19
	v_pk_mul_f32 v[18:19], v[28:29], s[20:21] op_sel_hi:[1,0]
	s_nop 0
	v_exp_f32_e32 v18, v18
	v_exp_f32_e32 v19, v19
	s_nop 0
	v_pk_add_f32 v[18:19], v[18:19], 1.0 op_sel_hi:[1,0]
	s_nop 0
	v_rcp_f32_e32 v96, v18
	v_mov_b32_e32 v18, 0
	v_cvt_pk_fp8_f32 v18, v22, v23
	v_rcp_f32_e32 v97, v19
	v_mov_b32_e32 v19, 0
	v_cvt_pk_fp8_f32 v19, v26, v27
	v_pk_mul_f32 v[22:23], v[28:29], v[30:31]
	v_cvt_pk_fp8_f32 v18, v24, v25 op_sel:[0,0,1]
	v_pk_fma_f32 v[24:25], v[92:93], s[18:19], v[12:13] op_sel_hi:[1,0,1]
	v_pk_mul_f32 v[22:23], v[22:23], v[96:97]
	v_min_f32_e32 v24, 0x40e00000, v24
	v_min_f32_e32 v25, 0x40e00000, v25
	v_cvt_pk_fp8_f32 v19, v22, v23 op_sel:[0,0,1]
	v_pk_mul_f32 v[26:27], v[24:25], s[20:21] op_sel_hi:[1,0]
	v_add_co_u32_e32 v22, vcc, s44, v20
	v_exp_f32_e32 v26, v26
	v_exp_f32_e32 v27, v27
	v_permlane16_swap_b32_e32 v16, v18
	v_permlane16_swap_b32_e32 v17, v19
	v_addc_co_u32_e32 v23, vcc, 0, v21, vcc
	global_store_dwordx4 v[22:23], v[16:19], off
	v_pk_fma_f32 v[28:29], v[82:83], s[18:19], v[2:3] op_sel_hi:[1,0,1]
	s_nop 0
	v_pk_add_f32 v[18:19], v[26:27], 1.0 op_sel_hi:[1,0]
	v_pk_fma_f32 v[16:17], v[88:89], s[18:19], v[8:9] op_sel_hi:[1,0,1]
	v_rcp_f32_e32 v18, v18
	v_rcp_f32_e32 v19, v19
	v_med3_f32 v16, v16, s76, v185
	v_med3_f32 v17, v17, s76, v185
	v_pk_fma_f32 v[16:17], v[16:17], 4.0, 4.0 op_sel_hi:[1,0,0]
	v_med3_f32 v28, v28, s76, v185
	v_pk_mul_f32 v[16:17], v[24:25], v[16:17]
	v_pk_fma_f32 v[24:25], v[90:91], s[18:19], v[10:11] op_sel_hi:[1,0,1]
	v_pk_mul_f32 v[18:19], v[16:17], v[18:19]
	v_pk_fma_f32 v[16:17], v[94:95], s[18:19], v[14:15] op_sel_hi:[1,0,1]
	v_med3_f32 v24, v24, s76, v185
	v_min_f32_e32 v16, 0x40e00000, v16
	v_min_f32_e32 v17, 0x40e00000, v17
	v_pk_mul_f32 v[22:23], v[16:17], s[20:21] op_sel_hi:[1,0]
	v_med3_f32 v25, v25, s76, v185
	v_exp_f32_e32 v22, v22
	v_exp_f32_e32 v23, v23
	v_pk_fma_f32 v[24:25], v[24:25], 4.0, 4.0 op_sel_hi:[1,0,0]
	v_med3_f32 v29, v29, s76, v185
	v_pk_mul_f32 v[16:17], v[16:17], v[24:25]
	v_pk_fma_f32 v[24:25], v[84:85], s[18:19], v[4:5] op_sel_hi:[1,0,1]
	v_pk_add_f32 v[22:23], v[22:23], 1.0 op_sel_hi:[1,0]
	v_min_f32_e32 v24, 0x40e00000, v24
	v_min_f32_e32 v25, 0x40e00000, v25
	v_pk_mul_f32 v[26:27], v[24:25], s[20:21] op_sel_hi:[1,0]
	v_rcp_f32_e32 v22, v22
	v_exp_f32_e32 v26, v26
	v_exp_f32_e32 v27, v27
	v_rcp_f32_e32 v23, v23
	v_pk_add_f32 v[26:27], v[26:27], 1.0 op_sel_hi:[1,0]
	v_pk_mul_f32 v[22:23], v[16:17], v[22:23]
	v_pk_fma_f32 v[16:17], v[80:81], s[18:19], v[0:1] op_sel_hi:[1,0,1]
	v_rcp_f32_e32 v26, v26
	v_rcp_f32_e32 v27, v27
	v_med3_f32 v16, v16, s76, v185
	v_med3_f32 v17, v17, s76, v185
	v_pk_fma_f32 v[16:17], v[16:17], 4.0, 4.0 op_sel_hi:[1,0,0]
	s_nop 0
	v_pk_mul_f32 v[16:17], v[24:25], v[16:17]
	s_nop 0
	v_pk_mul_f32 v[24:25], v[16:17], v[26:27]
	v_pk_fma_f32 v[16:17], v[86:87], s[18:19], v[6:7] op_sel_hi:[1,0,1]
	s_nop 0
	v_min_f32_e32 v26, 0x40e00000, v16
	v_min_f32_e32 v27, 0x40e00000, v17
	v_pk_mul_f32 v[16:17], v[26:27], s[20:21] op_sel_hi:[1,0]
	s_nop 0
	v_exp_f32_e32 v16, v16
	v_exp_f32_e32 v17, v17
	s_nop 0
	v_pk_add_f32 v[16:17], v[16:17], 1.0 op_sel_hi:[1,0]
	s_nop 0
	v_rcp_f32_e32 v30, v16
	v_mov_b32_e32 v16, 0
	v_cvt_pk_fp8_f32 v16, v18, v19
	v_rcp_f32_e32 v31, v17
	v_mov_b32_e32 v17, 0
	v_cvt_pk_fp8_f32 v17, v24, v25
	v_cvt_pk_fp8_f32 v16, v22, v23 op_sel:[0,0,1]
	v_pk_fma_f32 v[22:23], v[76:77], s[18:19], v[12:13] op_sel_hi:[1,0,1]
	v_pk_fma_f32 v[18:19], v[28:29], 4.0, 4.0 op_sel_hi:[1,0,0]
	v_min_f32_e32 v22, 0x40e00000, v22
	v_min_f32_e32 v23, 0x40e00000, v23
	v_pk_mul_f32 v[24:25], v[22:23], s[20:21] op_sel_hi:[1,0]
	v_pk_mul_f32 v[18:19], v[26:27], v[18:19]
	v_exp_f32_e32 v24, v24
	v_exp_f32_e32 v25, v25
	v_pk_mul_f32 v[18:19], v[18:19], v[30:31]
	v_pk_fma_f32 v[26:27], v[74:75], s[18:19], v[10:11] op_sel_hi:[1,0,1]
	v_cvt_pk_fp8_f32 v17, v18, v19 op_sel:[0,0,1]
	v_pk_add_f32 v[24:25], v[24:25], 1.0 op_sel_hi:[1,0]
	v_pk_fma_f32 v[18:19], v[72:73], s[18:19], v[8:9] op_sel_hi:[1,0,1]
	v_rcp_f32_e32 v24, v24
	v_rcp_f32_e32 v25, v25
	v_med3_f32 v18, v18, s76, v185
	v_med3_f32 v19, v19, s76, v185
	v_pk_fma_f32 v[18:19], v[18:19], 4.0, 4.0 op_sel_hi:[1,0,0]
	v_med3_f32 v26, v26, s76, v185
	v_pk_mul_f32 v[18:19], v[22:23], v[18:19]
	v_med3_f32 v27, v27, s76, v185
	v_pk_mul_f32 v[22:23], v[18:19], v[24:25]
	v_pk_fma_f32 v[18:19], v[78:79], s[18:19], v[14:15] op_sel_hi:[1,0,1]
	v_pk_fma_f32 v[26:27], v[26:27], 4.0, 4.0 op_sel_hi:[1,0,0]
	v_min_f32_e32 v18, 0x40e00000, v18
	v_min_f32_e32 v19, 0x40e00000, v19
	v_pk_mul_f32 v[24:25], v[18:19], s[20:21] op_sel_hi:[1,0]
	v_pk_mul_f32 v[18:19], v[18:19], v[26:27]
	v_exp_f32_e32 v24, v24
	v_exp_f32_e32 v25, v25
	v_pk_fma_f32 v[26:27], v[68:69], s[18:19], v[4:5] op_sel_hi:[1,0,1]
	v_pk_fma_f32 v[30:31], v[66:67], s[18:19], v[2:3] op_sel_hi:[1,0,1]
	v_min_f32_e32 v26, 0x40e00000, v26
	v_min_f32_e32 v27, 0x40e00000, v27
	v_pk_mul_f32 v[28:29], v[26:27], s[20:21] op_sel_hi:[1,0]
	v_pk_add_f32 v[24:25], v[24:25], 1.0 op_sel_hi:[1,0]
	v_exp_f32_e32 v28, v28
	v_exp_f32_e32 v29, v29
	v_rcp_f32_e32 v24, v24
	v_rcp_f32_e32 v25, v25
	v_med3_f32 v30, v30, s76, v185
	v_pk_add_f32 v[28:29], v[28:29], 1.0 op_sel_hi:[1,0]
	v_med3_f32 v31, v31, s76, v185
	v_pk_mul_f32 v[24:25], v[18:19], v[24:25]
	v_pk_fma_f32 v[18:19], v[64:65], s[18:19], v[0:1] op_sel_hi:[1,0,1]
	v_rcp_f32_e32 v28, v28
	v_rcp_f32_e32 v29, v29
	v_med3_f32 v18, v18, s76, v185
	v_med3_f32 v19, v19, s76, v185
	v_pk_fma_f32 v[18:19], v[18:19], 4.0, 4.0 op_sel_hi:[1,0,0]
	v_pk_fma_f32 v[30:31], v[30:31], 4.0, 4.0 op_sel_hi:[1,0,0]
	v_pk_mul_f32 v[18:19], v[26:27], v[18:19]
	s_nop 0
	v_pk_mul_f32 v[26:27], v[18:19], v[28:29]
	v_pk_fma_f32 v[18:19], v[70:71], s[18:19], v[6:7] op_sel_hi:[1,0,1]
	s_nop 0
	v_min_f32_e32 v28, 0x40e00000, v18
	v_min_f32_e32 v29, 0x40e00000, v19
	v_pk_mul_f32 v[18:19], v[28:29], s[20:21] op_sel_hi:[1,0]
	s_nop 0
	v_exp_f32_e32 v18, v18
	v_exp_f32_e32 v19, v19
	s_nop 0
	v_pk_add_f32 v[18:19], v[18:19], 1.0 op_sel_hi:[1,0]
	s_nop 0
	v_rcp_f32_e32 v64, v18
	v_rcp_f32_e32 v65, v19
	v_mov_b32_e32 v19, 0
	v_cvt_pk_fp8_f32 v19, v26, v27
	v_mov_b32_e32 v18, 0
	v_cvt_pk_fp8_f32 v18, v22, v23
	v_pk_mul_f32 v[22:23], v[28:29], v[30:31]
	v_add_co_u32_e32 v26, vcc, s77, v20
	v_pk_mul_f32 v[22:23], v[22:23], v[64:65]
	v_cvt_pk_fp8_f32 v18, v24, v25 op_sel:[0,0,1]
	v_cvt_pk_fp8_f32 v19, v22, v23 op_sel:[0,0,1]
	v_pk_fma_f32 v[22:23], v[36:37], s[18:19], v[4:5] op_sel_hi:[1,0,1]
	v_addc_co_u32_e32 v27, vcc, 0, v21, vcc
	v_min_f32_e32 v22, 0x40e00000, v22
	v_min_f32_e32 v23, 0x40e00000, v23
	v_pk_mul_f32 v[24:25], v[22:23], s[20:21] op_sel_hi:[1,0]
	v_permlane16_swap_b32_e32 v16, v18
	v_exp_f32_e32 v24, v24
	v_exp_f32_e32 v25, v25
	v_permlane16_swap_b32_e32 v17, v19
	global_store_dwordx4 v[26:27], v[16:19], off
	v_pk_fma_f32 v[4:5], v[52:53], s[18:19], v[4:5] op_sel_hi:[1,0,1]
	s_nop 0
	v_pk_add_f32 v[16:17], v[24:25], 1.0 op_sel_hi:[1,0]
	v_pk_fma_f32 v[24:25], v[62:63], s[18:19], v[14:15] op_sel_hi:[1,0,1]
	v_rcp_f32_e32 v16, v16
	v_min_f32_e32 v24, 0x40e00000, v24
	v_min_f32_e32 v25, 0x40e00000, v25
	v_pk_mul_f32 v[26:27], v[24:25], s[20:21] op_sel_hi:[1,0]
	v_rcp_f32_e32 v17, v17
	v_pk_fma_f32 v[18:19], v[32:33], s[18:19], v[0:1] op_sel_hi:[1,0,1]
	v_exp_f32_e32 v26, v26
	v_exp_f32_e32 v27, v27
	v_med3_f32 v18, v18, s76, v185
	v_med3_f32 v19, v19, s76, v185
	v_pk_fma_f32 v[18:19], v[18:19], 4.0, 4.0 op_sel_hi:[1,0,0]
	v_min_f32_e32 v4, 0x40e00000, v4
	v_pk_mul_f32 v[18:19], v[22:23], v[18:19]
	v_pk_fma_f32 v[22:23], v[58:59], s[18:19], v[10:11] op_sel_hi:[1,0,1]
	v_pk_mul_f32 v[16:17], v[18:19], v[16:17]
	v_pk_add_f32 v[18:19], v[26:27], 1.0 op_sel_hi:[1,0]
	v_pk_fma_f32 v[26:27], v[60:61], s[18:19], v[12:13] op_sel_hi:[1,0,1]
	v_rcp_f32_e32 v18, v18
	v_min_f32_e32 v26, 0x40e00000, v26
	v_min_f32_e32 v27, 0x40e00000, v27
	v_pk_mul_f32 v[28:29], v[26:27], s[20:21] op_sel_hi:[1,0]
	v_rcp_f32_e32 v19, v19
	v_exp_f32_e32 v28, v28
	v_exp_f32_e32 v29, v29
	v_med3_f32 v22, v22, s76, v185
	v_med3_f32 v23, v23, s76, v185
	v_pk_fma_f32 v[22:23], v[22:23], 4.0, 4.0 op_sel_hi:[1,0,0]
	v_min_f32_e32 v5, 0x40e00000, v5
	v_pk_mul_f32 v[22:23], v[24:25], v[22:23]
	v_pk_fma_f32 v[24:25], v[56:57], s[18:19], v[8:9] op_sel_hi:[1,0,1]
	v_pk_mul_f32 v[18:19], v[22:23], v[18:19]
	v_pk_add_f32 v[22:23], v[28:29], 1.0 op_sel_hi:[1,0]
	v_pk_fma_f32 v[28:29], v[54:55], s[18:19], v[6:7] op_sel_hi:[1,0,1]
	v_rcp_f32_e32 v22, v22
	v_min_f32_e32 v28, 0x40e00000, v28
	v_min_f32_e32 v29, 0x40e00000, v29
	v_pk_mul_f32 v[30:31], v[28:29], s[20:21] op_sel_hi:[1,0]
	v_rcp_f32_e32 v23, v23
	v_exp_f32_e32 v30, v30
	v_exp_f32_e32 v31, v31
	v_med3_f32 v24, v24, s76, v185
	v_med3_f32 v25, v25, s76, v185
	v_pk_fma_f32 v[24:25], v[24:25], 4.0, 4.0 op_sel_hi:[1,0,0]
	v_pk_fma_f32 v[0:1], v[48:49], s[18:19], v[0:1] op_sel_hi:[1,0,1]
	v_pk_mul_f32 v[24:25], v[26:27], v[24:25]
	v_med3_f32 v0, v0, s76, v185
	v_pk_mul_f32 v[22:23], v[24:25], v[22:23]
	v_pk_add_f32 v[24:25], v[30:31], 1.0 op_sel_hi:[1,0]
	v_pk_mul_f32 v[30:31], v[4:5], s[20:21] op_sel_hi:[1,0]
	v_med3_f32 v1, v1, s76, v185
	v_exp_f32_e32 v30, v30
	v_exp_f32_e32 v31, v31
	v_pk_fma_f32 v[0:1], v[0:1], 4.0, 4.0 op_sel_hi:[1,0,0]
	v_rcp_f32_e32 v24, v24
	v_pk_mul_f32 v[0:1], v[4:5], v[0:1]
	v_pk_add_f32 v[30:31], v[30:31], 1.0 op_sel_hi:[1,0]
	v_rcp_f32_e32 v25, v25
	v_rcp_f32_e32 v30, v30
	v_rcp_f32_e32 v31, v31
	v_pk_fma_f32 v[26:27], v[50:51], s[18:19], v[2:3] op_sel_hi:[1,0,1]
	v_pk_fma_f32 v[12:13], v[44:45], s[18:19], v[12:13] op_sel_hi:[1,0,1]
	v_med3_f32 v26, v26, s76, v185
	v_pk_mul_f32 v[4:5], v[0:1], v[30:31]
	v_mov_b32_e32 v1, 0
	v_med3_f32 v27, v27, s76, v185
	v_cvt_pk_fp8_f32 v1, v4, v5
	v_pk_fma_f32 v[26:27], v[26:27], 4.0, 4.0 op_sel_hi:[1,0,0]
	v_min_f32_e32 v12, 0x40e00000, v12
	v_pk_mul_f32 v[26:27], v[28:29], v[26:27]
	v_min_f32_e32 v13, 0x40e00000, v13
	v_pk_mul_f32 v[24:25], v[26:27], v[24:25]
	v_pk_fma_f32 v[4:5], v[46:47], s[18:19], v[14:15] op_sel_hi:[1,0,1]
	v_cvt_pk_fp8_f32 v1, v24, v25 op_sel:[0,0,1]
	v_pk_mul_f32 v[24:25], v[12:13], s[20:21] op_sel_hi:[1,0]
	v_min_f32_e32 v4, 0x40e00000, v4
	v_exp_f32_e32 v24, v24
	v_exp_f32_e32 v25, v25
	v_min_f32_e32 v5, 0x40e00000, v5
	v_pk_mul_f32 v[14:15], v[4:5], s[20:21] op_sel_hi:[1,0]
	v_pk_fma_f32 v[8:9], v[40:41], s[18:19], v[8:9] op_sel_hi:[1,0,1]
	v_exp_f32_e32 v14, v14
	v_exp_f32_e32 v15, v15
	v_pk_add_f32 v[24:25], v[24:25], 1.0 op_sel_hi:[1,0]
	v_med3_f32 v8, v8, s76, v185
	v_rcp_f32_e32 v24, v24
	v_rcp_f32_e32 v25, v25
	v_med3_f32 v9, v9, s76, v185
	v_pk_fma_f32 v[8:9], v[8:9], 4.0, 4.0 op_sel_hi:[1,0,0]
	v_pk_add_f32 v[14:15], v[14:15], 1.0 op_sel_hi:[1,0]
	v_pk_mul_f32 v[8:9], v[12:13], v[8:9]
	v_rcp_f32_e32 v14, v14
	v_rcp_f32_e32 v15, v15
	v_pk_fma_f32 v[10:11], v[42:43], s[18:19], v[10:11] op_sel_hi:[1,0,1]
	v_pk_mul_f32 v[8:9], v[8:9], v[24:25]
	v_mov_b32_e32 v0, 0
	v_med3_f32 v10, v10, s76, v185
	v_med3_f32 v11, v11, s76, v185
	v_cvt_pk_fp8_f32 v0, v8, v9
	v_pk_fma_f32 v[8:9], v[10:11], 4.0, 4.0 op_sel_hi:[1,0,0]
	v_pk_fma_f32 v[2:3], v[34:35], s[18:19], v[2:3] op_sel_hi:[1,0,1]
	v_pk_mul_f32 v[4:5], v[4:5], v[8:9]
	v_med3_f32 v2, v2, s76, v185
	v_pk_mul_f32 v[4:5], v[4:5], v[14:15]
	v_med3_f32 v3, v3, s76, v185
	v_cvt_pk_fp8_f32 v0, v4, v5 op_sel:[0,0,1]
	v_pk_fma_f32 v[4:5], v[38:39], s[18:19], v[6:7] op_sel_hi:[1,0,1]
	v_pk_fma_f32 v[8:9], v[2:3], 4.0, 4.0 op_sel_hi:[1,0,0]
	v_min_f32_e32 v4, 0x40e00000, v4
	v_min_f32_e32 v5, 0x40e00000, v5
	v_pk_mul_f32 v[6:7], v[4:5], s[20:21] op_sel_hi:[1,0]
	v_mov_b32_e32 v2, 0
	v_exp_f32_e32 v6, v6
	v_exp_f32_e32 v7, v7
	v_mov_b32_e32 v3, 0
	v_cvt_pk_fp8_f32 v2, v22, v23
	v_cvt_pk_fp8_f32 v3, v16, v17
	v_pk_add_f32 v[6:7], v[6:7], 1.0 op_sel_hi:[1,0]
	v_pk_mul_f32 v[4:5], v[4:5], v[8:9]
	v_rcp_f32_e32 v6, v6
	v_rcp_f32_e32 v7, v7
	v_cvt_pk_fp8_f32 v2, v18, v19 op_sel:[0,0,1]
	v_pk_mul_f32 v[4:5], v[4:5], v[6:7]
	s_nop 0
	v_cvt_pk_fp8_f32 v3, v4, v5 op_sel:[0,0,1]
	v_add_co_u32_e32 v4, vcc, 0x50000, v20
	v_permlane16_swap_b32_e32 v0, v2
	s_nop 0
	v_addc_co_u32_e32 v5, vcc, 0, v21, vcc
	v_permlane16_swap_b32_e32 v1, v3
	s_and_b64 vcc, exec, s[6:7]
	s_mov_b64 s[6:7], -1
	global_store_dwordx4 v[4:5], v[0:3], off
	s_cbranch_vccnz .LBB0_2264
	s_andn2_b64 vcc, exec, s[12:13]
	s_cbranch_vccnz .LBB0_2263
	s_barrier
	s_branch .LBB0_2263
